# lean attention loop: one LDS wait per two fragments, fragment lookahead 8, priority raise only for waves 4-7 in the first tile of a block
# speedup vs baseline: 1.0034x; 1.0034x over previous
.Lattn_pa0:
	s_waitcnt lgkmcnt(6)
	v_mfma_f32_16x16x32_bf16 v[64:67], v[160:163], v[96:99], 0
	v_exp_f32_e32 v88, v88
	v_mfma_f32_16x16x32_bf16 v[68:71], v[160:163], v[112:115], 0
	v_exp_f32_e32 v92, v92
	ds_read_b128 v[160:163], v201 offset:20480
	s_add_u32 s16, s22, s10
	s_addc_u32 s17, s23, s11
	s_add_u32 s15, s22, s12
	s_addc_u32 s14, s23, s13
	s_add_u32 s8, s16, 0x3bc00200
	s_addc_u32 s9, s17, 0
	s_add_u32 s6, s15, 0x23a50000
	s_addc_u32 s7, s14, 0
	v_mfma_f32_16x16x32_bf16 v[0:3], v[164:167], v[216:219], v[0:3]
	v_cvt_pk_bf16_f32 v242, v80, v81
	v_mfma_f32_16x16x32_bf16 v[4:7], v[164:167], v[238:241], v[4:7]
	v_exp_f32_e32 v89, v89
	ds_read_b128 v[164:167], v209 offset:8192
	s_waitcnt vmcnt(4)
	ds_write_b128 v225, v[152:155] offset:49152
	s_waitcnt lgkmcnt(7)
	v_mfma_f32_16x16x32_bf16 v[68:71], v[168:171], v[116:119], v[68:71]
	v_exp_f32_e32 v93, v93
	v_mfma_f32_16x16x32_bf16 v[64:67], v[168:171], v[100:103], v[64:67]
	v_cvt_pk_bf16_f32 v243, v82, v83
	ds_read_b128 v[168:171], v202 offset:20480
	ds_write_b128 v226, v[156:159] offset:49152
	v_mfma_f32_16x16x32_bf16 v[12:15], v[172:175], v[238:241], v[12:15]
	v_exp_f32_e32 v90, v90
	v_mfma_f32_16x16x32_bf16 v[8:11], v[172:175], v[216:219], v[8:11]
	v_exp_f32_e32 v94, v94
	ds_read_b128 v[172:175], v209 offset:10240
	ds_write_b64 v227, v[132:133] offset:32768
	s_waitcnt lgkmcnt(9)
	v_mfma_f32_16x16x32_bf16 v[64:67], v[176:179], v[104:107], v[64:67]
	v_cvt_pk_bf16_f32 v204, v84, v85
	v_mfma_f32_16x16x32_bf16 v[68:71], v[176:179], v[120:123], v[68:71]
	v_exp_f32_e32 v91, v91
	ds_read_b128 v[176:179], v203 offset:20480
	ds_write_b64 v228, v[134:135] offset:32768
	v_mfma_f32_16x16x32_bf16 v[16:19], v[180:183], v[216:219], v[16:19]
	v_exp_f32_e32 v95, v95
	v_mfma_f32_16x16x32_bf16 v[20:23], v[180:183], v[238:241], v[20:23]
	v_cvt_pk_bf16_f32 v205, v86, v87
	v_add_f32_e32 v220, v220, v88
	ds_read_b128 v[180:183], v209 offset:12288
	ds_write_b64 v229, v[128:129] offset:32768
	s_waitcnt lgkmcnt(11)
	v_mfma_f32_16x16x32_bf16 v[68:71], v[230:233], v[124:127], v[68:71]
	v_add_f32_e32 v221, v221, v92
	v_add_f32_e32 v220, v220, v89
	v_mfma_f32_16x16x32_bf16 v[64:67], v[230:233], v[108:111], v[64:67]
	v_add_f32_e32 v221, v221, v93
	v_cvt_pk_bf16_f32 v244, v88, v89
	ds_read_b128 v[230:233], v246 offset:20480
	ds_write_b64 v184, v[130:131] offset:32768
	v_mfma_f32_16x16x32_bf16 v[28:31], v[234:237], v[238:241], v[28:31]
	v_cvt_pk_bf16_f32 v245, v90, v91
	v_cvt_pk_bf16_f32 v206, v92, v93
	v_mfma_f32_16x16x32_bf16 v[24:27], v[234:237], v[216:219], v[24:27]
	v_cvt_pk_bf16_f32 v207, v94, v95
	ds_read_b128 v[234:237], v209 offset:14336
	global_load_dwordx4 v[132:135], v198, s[8:9]
	s_waitcnt lgkmcnt(12)
	v_mfma_f32_16x16x32_bf16 v[72:75], v[160:163], v[96:99], 0
	v_add_f32_e32 v220, v220, v90
	v_add_f32_e32 v221, v221, v94
	v_mfma_f32_16x16x32_bf16 v[76:79], v[160:163], v[112:115], 0
	v_add_f32_e32 v220, v220, v91
	v_add_f32_e32 v221, v221, v95
	ds_read_b128 v[160:163], v201 offset:24576
	global_load_dwordx4 v[128:131], v199, s[8:9]
	v_mfma_f32_16x16x32_bf16 v[32:35], v[164:167], v[216:219], v[32:35]
	v_add_f32_e32 v194, v194, v220
	v_add_f32_e32 v195, v195, v221
	v_mfma_f32_16x16x32_bf16 v[36:39], v[164:167], v[238:241], v[36:39]
	v_exp_f32_e32 v64, v64
	ds_read_b128 v[164:167], v210 offset:0
	global_load_dwordx4 v[152:155], v196, s[6:7]
	s_waitcnt lgkmcnt(10)
	v_mfma_f32_16x16x32_bf16 v[76:79], v[168:171], v[116:119], v[76:79]
	v_exp_f32_e32 v68, v68
	v_mfma_f32_16x16x32_bf16 v[72:75], v[168:171], v[100:103], v[72:75]
	v_exp_f32_e32 v65, v65
	ds_read_b128 v[168:171], v202 offset:24576
	global_load_dwordx4 v[156:159], v197, s[6:7]
	v_mfma_f32_16x16x32_bf16 v[44:47], v[172:175], v[238:241], v[44:47]
	v_exp_f32_e32 v69, v69
	v_mfma_f32_16x16x32_bf16 v[40:43], v[172:175], v[216:219], v[40:43]
	v_exp_f32_e32 v66, v66
	ds_read_b128 v[172:175], v210 offset:2048
	s_waitcnt lgkmcnt(8)
	v_mfma_f32_16x16x32_bf16 v[72:75], v[176:179], v[104:107], v[72:75]
	v_exp_f32_e32 v70, v70
	v_mfma_f32_16x16x32_bf16 v[76:79], v[176:179], v[120:123], v[76:79]
	v_exp_f32_e32 v67, v67
	ds_read_b128 v[176:179], v203 offset:24576
	v_mfma_f32_16x16x32_bf16 v[48:51], v[180:183], v[216:219], v[48:51]
	v_exp_f32_e32 v71, v71
	v_mfma_f32_16x16x32_bf16 v[52:55], v[180:183], v[238:241], v[52:55]
	v_add_f32_e32 v220, v64, v65
	ds_read_b128 v[180:183], v210 offset:4096
	s_waitcnt lgkmcnt(6)
	v_mfma_f32_16x16x32_bf16 v[76:79], v[230:233], v[124:127], v[76:79]
	v_add_f32_e32 v221, v68, v69
	v_mfma_f32_16x16x32_bf16 v[72:75], v[230:233], v[108:111], v[72:75]
	v_add_f32_e32 v220, v220, v66
	ds_read_b128 v[230:233], v246 offset:24576
	v_mfma_f32_16x16x32_bf16 v[60:63], v[234:237], v[238:241], v[60:63]
	v_add_f32_e32 v221, v221, v70
	v_add_f32_e32 v220, v220, v67
	v_mfma_f32_16x16x32_bf16 v[56:59], v[234:237], v[216:219], v[56:59]
	v_add_f32_e32 v221, v221, v71
	ds_read_b128 v[234:237], v210 offset:6144
	s_waitcnt lgkmcnt(6)
	v_mfma_f32_16x16x32_bf16 v[80:83], v[160:163], v[96:99], 0
	v_exp_f32_e32 v72, v72
	v_mfma_f32_16x16x32_bf16 v[84:87], v[160:163], v[112:115], 0
	v_exp_f32_e32 v76, v76
	ds_read_b128 v[160:163], v201 offset:28672
	v_mfma_f32_16x16x32_bf16 v[0:3], v[164:167], v[242:245], v[0:3]
	v_exp_f32_e32 v73, v73
	v_mfma_f32_16x16x32_bf16 v[4:7], v[164:167], v[204:207], v[4:7]
	v_exp_f32_e32 v77, v77
	ds_read_b128 v[164:167], v210 offset:8192
	s_waitcnt lgkmcnt(6)
	v_mfma_f32_16x16x32_bf16 v[84:87], v[168:171], v[116:119], v[84:87]
	v_exp_f32_e32 v74, v74
	v_mfma_f32_16x16x32_bf16 v[80:83], v[168:171], v[100:103], v[80:83]
	v_exp_f32_e32 v78, v78
	ds_read_b128 v[168:171], v202 offset:28672
	v_mfma_f32_16x16x32_bf16 v[12:15], v[172:175], v[204:207], v[12:15]
	v_exp_f32_e32 v75, v75
	v_mfma_f32_16x16x32_bf16 v[8:11], v[172:175], v[242:245], v[8:11]
	v_exp_f32_e32 v79, v79
	ds_read_b128 v[172:175], v210 offset:10240
	s_waitcnt lgkmcnt(6)
	v_mfma_f32_16x16x32_bf16 v[80:83], v[176:179], v[104:107], v[80:83]
	v_add_f32_e32 v220, v220, v72
	v_add_f32_e32 v221, v221, v76
	v_mfma_f32_16x16x32_bf16 v[84:87], v[176:179], v[120:123], v[84:87]
	v_add_f32_e32 v220, v220, v73
	ds_read_b128 v[176:179], v203 offset:28672
	v_mfma_f32_16x16x32_bf16 v[16:19], v[180:183], v[242:245], v[16:19]
	v_add_f32_e32 v221, v221, v77
	v_add_f32_e32 v220, v220, v74
	v_mfma_f32_16x16x32_bf16 v[20:23], v[180:183], v[204:207], v[20:23]
	v_add_f32_e32 v221, v221, v78
	ds_read_b128 v[180:183], v210 offset:12288
	s_waitcnt lgkmcnt(6)
	v_mfma_f32_16x16x32_bf16 v[84:87], v[230:233], v[124:127], v[84:87]
	v_add_f32_e32 v220, v220, v75
	v_add_f32_e32 v221, v221, v79
	v_mfma_f32_16x16x32_bf16 v[80:83], v[230:233], v[108:111], v[80:83]
	v_cvt_pk_bf16_f32 v216, v64, v65
	ds_read_b128 v[230:233], v246 offset:28672
	v_mfma_f32_16x16x32_bf16 v[28:31], v[234:237], v[204:207], v[28:31]
	v_cvt_pk_bf16_f32 v217, v66, v67
	v_cvt_pk_bf16_f32 v238, v68, v69
	v_mfma_f32_16x16x32_bf16 v[24:27], v[234:237], v[242:245], v[24:27]
	v_cvt_pk_bf16_f32 v239, v70, v71
	ds_read_b128 v[234:237], v210 offset:14336
	s_waitcnt lgkmcnt(6)
	v_mfma_f32_16x16x32_bf16 v[88:91], v[160:163], v[96:99], 0
	v_exp_f32_e32 v80, v80
	v_mfma_f32_16x16x32_bf16 v[92:95], v[160:163], v[112:115], 0
	v_exp_f32_e32 v84, v84
	ds_read_b128 v[160:163], v201 offset:32768
	v_mfma_f32_16x16x32_bf16 v[32:35], v[164:167], v[242:245], v[32:35]
	v_exp_f32_e32 v81, v81
	v_mfma_f32_16x16x32_bf16 v[36:39], v[164:167], v[204:207], v[36:39]
	v_exp_f32_e32 v85, v85
	ds_read_b128 v[164:167], v209 offset:16384
	s_waitcnt lgkmcnt(6)
	v_mfma_f32_16x16x32_bf16 v[92:95], v[168:171], v[116:119], v[92:95]
	v_exp_f32_e32 v82, v82
	v_mfma_f32_16x16x32_bf16 v[88:91], v[168:171], v[100:103], v[88:91]
	v_exp_f32_e32 v86, v86
	ds_read_b128 v[168:171], v202 offset:32768
	v_mfma_f32_16x16x32_bf16 v[44:47], v[172:175], v[204:207], v[44:47]
	v_exp_f32_e32 v83, v83
	v_mfma_f32_16x16x32_bf16 v[40:43], v[172:175], v[242:245], v[40:43]
	v_exp_f32_e32 v87, v87
	ds_read_b128 v[172:175], v209 offset:18432
	s_waitcnt lgkmcnt(6)
	v_mfma_f32_16x16x32_bf16 v[88:91], v[176:179], v[104:107], v[88:91]
	v_add_f32_e32 v220, v220, v80
	v_add_f32_e32 v221, v221, v84
	v_mfma_f32_16x16x32_bf16 v[92:95], v[176:179], v[120:123], v[92:95]
	v_add_f32_e32 v220, v220, v81
	ds_read_b128 v[176:179], v203 offset:32768
	v_mfma_f32_16x16x32_bf16 v[48:51], v[180:183], v[242:245], v[48:51]
	v_add_f32_e32 v221, v221, v85
	v_add_f32_e32 v220, v220, v82
	v_mfma_f32_16x16x32_bf16 v[52:55], v[180:183], v[204:207], v[52:55]
	v_add_f32_e32 v221, v221, v86
	ds_read_b128 v[180:183], v209 offset:20480
	s_waitcnt lgkmcnt(6)
	v_mfma_f32_16x16x32_bf16 v[92:95], v[230:233], v[124:127], v[92:95]
	v_add_f32_e32 v220, v220, v83
	v_add_f32_e32 v221, v221, v87
	v_mfma_f32_16x16x32_bf16 v[88:91], v[230:233], v[108:111], v[88:91]
	v_cvt_pk_bf16_f32 v218, v72, v73
	ds_read_b128 v[230:233], v246 offset:32768
	v_mfma_f32_16x16x32_bf16 v[60:63], v[234:237], v[204:207], v[60:63]
	v_cvt_pk_bf16_f32 v219, v74, v75
	v_cvt_pk_bf16_f32 v240, v76, v77
	v_mfma_f32_16x16x32_bf16 v[56:59], v[234:237], v[242:245], v[56:59]
	v_cvt_pk_bf16_f32 v241, v78, v79
	ds_read_b128 v[234:237], v209 offset:22528
	s_setprio 0
	s_waitcnt lgkmcnt(6)
	v_mfma_f32_16x16x32_bf16 v[64:67], v[160:163], v[96:99], 0
	v_exp_f32_e32 v88, v88
	v_mfma_f32_16x16x32_bf16 v[68:71], v[160:163], v[112:115], 0
	v_exp_f32_e32 v92, v92
	ds_read_b128 v[160:163], v201 offset:36864
	s_add_u32 s8, s16, 0x3bc00280
	s_addc_u32 s9, s17, 0
	s_add_u32 s6, s15, 0x23a60000
	s_addc_u32 s7, s14, 0
	v_mfma_f32_16x16x32_bf16 v[0:3], v[164:167], v[216:219], v[0:3]
	v_cvt_pk_bf16_f32 v242, v80, v81
	v_mfma_f32_16x16x32_bf16 v[4:7], v[164:167], v[238:241], v[4:7]
	v_exp_f32_e32 v89, v89
	ds_read_b128 v[164:167], v209 offset:24576
	s_waitcnt vmcnt(4)
	ds_write_b128 v225, v[136:139] offset:0
	s_waitcnt lgkmcnt(7)
	v_mfma_f32_16x16x32_bf16 v[68:71], v[168:171], v[116:119], v[68:71]
	v_exp_f32_e32 v93, v93
	v_mfma_f32_16x16x32_bf16 v[64:67], v[168:171], v[100:103], v[64:67]
	v_cvt_pk_bf16_f32 v243, v82, v83
	ds_read_b128 v[168:171], v202 offset:36864
	ds_write_b128 v226, v[140:143] offset:0
	v_mfma_f32_16x16x32_bf16 v[12:15], v[172:175], v[238:241], v[12:15]
	v_exp_f32_e32 v90, v90
	v_mfma_f32_16x16x32_bf16 v[8:11], v[172:175], v[216:219], v[8:11]
	v_exp_f32_e32 v94, v94
	ds_read_b128 v[172:175], v209 offset:26624
	ds_write_b64 v227, v[148:149] offset:49152
	s_waitcnt lgkmcnt(9)
	v_mfma_f32_16x16x32_bf16 v[64:67], v[176:179], v[104:107], v[64:67]
	v_cvt_pk_bf16_f32 v204, v84, v85
	v_mfma_f32_16x16x32_bf16 v[68:71], v[176:179], v[120:123], v[68:71]
	v_exp_f32_e32 v91, v91
	ds_read_b128 v[176:179], v203 offset:36864
	ds_write_b64 v228, v[150:151] offset:49152
	v_mfma_f32_16x16x32_bf16 v[16:19], v[180:183], v[216:219], v[16:19]
	v_exp_f32_e32 v95, v95
	v_mfma_f32_16x16x32_bf16 v[20:23], v[180:183], v[238:241], v[20:23]
	v_cvt_pk_bf16_f32 v205, v86, v87
	v_add_f32_e32 v220, v220, v88
	ds_read_b128 v[180:183], v209 offset:28672
	ds_write_b64 v229, v[144:145] offset:49152
	s_waitcnt lgkmcnt(11)
	v_mfma_f32_16x16x32_bf16 v[68:71], v[230:233], v[124:127], v[68:71]
	v_add_f32_e32 v221, v221, v92
	v_add_f32_e32 v220, v220, v89
	v_mfma_f32_16x16x32_bf16 v[64:67], v[230:233], v[108:111], v[64:67]
	v_add_f32_e32 v221, v221, v93
	v_cvt_pk_bf16_f32 v244, v88, v89
	ds_read_b128 v[230:233], v246 offset:36864
	ds_write_b64 v184, v[146:147] offset:49152
	v_mfma_f32_16x16x32_bf16 v[28:31], v[234:237], v[238:241], v[28:31]
	v_cvt_pk_bf16_f32 v245, v90, v91
	v_cvt_pk_bf16_f32 v206, v92, v93
	v_mfma_f32_16x16x32_bf16 v[24:27], v[234:237], v[216:219], v[24:27]
	v_cvt_pk_bf16_f32 v207, v94, v95
	ds_read_b128 v[234:237], v209 offset:30720
	global_load_dwordx4 v[148:151], v198, s[8:9]
	s_waitcnt lgkmcnt(12)
	v_mfma_f32_16x16x32_bf16 v[72:75], v[160:163], v[96:99], 0
	v_add_f32_e32 v220, v220, v90
	v_add_f32_e32 v221, v221, v94
	v_mfma_f32_16x16x32_bf16 v[76:79], v[160:163], v[112:115], 0
	v_add_f32_e32 v220, v220, v91
	v_add_f32_e32 v221, v221, v95
	ds_read_b128 v[160:163], v201 offset:40960
	global_load_dwordx4 v[144:147], v199, s[8:9]
	v_mfma_f32_16x16x32_bf16 v[32:35], v[164:167], v[216:219], v[32:35]
	v_add_f32_e32 v194, v194, v220
	v_add_f32_e32 v195, v195, v221
	v_mfma_f32_16x16x32_bf16 v[36:39], v[164:167], v[238:241], v[36:39]
	v_exp_f32_e32 v64, v64
	ds_read_b128 v[164:167], v210 offset:16384
	global_load_dwordx4 v[136:139], v196, s[6:7]
	s_waitcnt lgkmcnt(10)
	v_mfma_f32_16x16x32_bf16 v[76:79], v[168:171], v[116:119], v[76:79]
	v_exp_f32_e32 v68, v68
	v_mfma_f32_16x16x32_bf16 v[72:75], v[168:171], v[100:103], v[72:75]
	v_exp_f32_e32 v65, v65
	ds_read_b128 v[168:171], v202 offset:40960
	global_load_dwordx4 v[140:143], v197, s[6:7]
	v_mfma_f32_16x16x32_bf16 v[44:47], v[172:175], v[238:241], v[44:47]
	v_exp_f32_e32 v69, v69
	v_mfma_f32_16x16x32_bf16 v[40:43], v[172:175], v[216:219], v[40:43]
	v_exp_f32_e32 v66, v66
	ds_read_b128 v[172:175], v210 offset:18432
	s_waitcnt lgkmcnt(8)
	v_mfma_f32_16x16x32_bf16 v[72:75], v[176:179], v[104:107], v[72:75]
	v_exp_f32_e32 v70, v70
	v_mfma_f32_16x16x32_bf16 v[76:79], v[176:179], v[120:123], v[76:79]
	v_exp_f32_e32 v67, v67
	ds_read_b128 v[176:179], v203 offset:40960
	v_mfma_f32_16x16x32_bf16 v[48:51], v[180:183], v[216:219], v[48:51]
	v_exp_f32_e32 v71, v71
	v_mfma_f32_16x16x32_bf16 v[52:55], v[180:183], v[238:241], v[52:55]
	v_add_f32_e32 v220, v64, v65
	ds_read_b128 v[180:183], v210 offset:20480
	s_waitcnt lgkmcnt(6)
	v_mfma_f32_16x16x32_bf16 v[76:79], v[230:233], v[124:127], v[76:79]
	v_add_f32_e32 v221, v68, v69
	v_mfma_f32_16x16x32_bf16 v[72:75], v[230:233], v[108:111], v[72:75]
	v_add_f32_e32 v220, v220, v66
	ds_read_b128 v[230:233], v246 offset:40960
	v_mfma_f32_16x16x32_bf16 v[60:63], v[234:237], v[238:241], v[60:63]
	v_add_f32_e32 v221, v221, v70
	v_add_f32_e32 v220, v220, v67
	v_mfma_f32_16x16x32_bf16 v[56:59], v[234:237], v[216:219], v[56:59]
	v_add_f32_e32 v221, v221, v71
	ds_read_b128 v[234:237], v210 offset:22528
	s_waitcnt lgkmcnt(6)
	v_mfma_f32_16x16x32_bf16 v[80:83], v[160:163], v[96:99], 0
	v_exp_f32_e32 v72, v72
	v_mfma_f32_16x16x32_bf16 v[84:87], v[160:163], v[112:115], 0
	v_exp_f32_e32 v76, v76
	ds_read_b128 v[160:163], v201 offset:45056
	v_mfma_f32_16x16x32_bf16 v[0:3], v[164:167], v[242:245], v[0:3]
	v_exp_f32_e32 v73, v73
	v_mfma_f32_16x16x32_bf16 v[4:7], v[164:167], v[204:207], v[4:7]
	v_exp_f32_e32 v77, v77
	ds_read_b128 v[164:167], v210 offset:24576
	s_waitcnt lgkmcnt(6)
	v_mfma_f32_16x16x32_bf16 v[84:87], v[168:171], v[116:119], v[84:87]
	v_exp_f32_e32 v74, v74
	v_mfma_f32_16x16x32_bf16 v[80:83], v[168:171], v[100:103], v[80:83]
	v_exp_f32_e32 v78, v78
	ds_read_b128 v[168:171], v202 offset:45056
	v_mfma_f32_16x16x32_bf16 v[12:15], v[172:175], v[204:207], v[12:15]
	v_exp_f32_e32 v75, v75
	v_mfma_f32_16x16x32_bf16 v[8:11], v[172:175], v[242:245], v[8:11]
	v_exp_f32_e32 v79, v79
	ds_read_b128 v[172:175], v210 offset:26624
	s_waitcnt lgkmcnt(6)
	v_mfma_f32_16x16x32_bf16 v[80:83], v[176:179], v[104:107], v[80:83]
	v_add_f32_e32 v220, v220, v72
	v_add_f32_e32 v221, v221, v76
	v_mfma_f32_16x16x32_bf16 v[84:87], v[176:179], v[120:123], v[84:87]
	v_add_f32_e32 v220, v220, v73
	ds_read_b128 v[176:179], v203 offset:45056
	v_mfma_f32_16x16x32_bf16 v[16:19], v[180:183], v[242:245], v[16:19]
	v_add_f32_e32 v221, v221, v77
	v_add_f32_e32 v220, v220, v74
	v_mfma_f32_16x16x32_bf16 v[20:23], v[180:183], v[204:207], v[20:23]
	v_add_f32_e32 v221, v221, v78
	ds_read_b128 v[180:183], v210 offset:28672
	s_waitcnt lgkmcnt(6)
	v_mfma_f32_16x16x32_bf16 v[84:87], v[230:233], v[124:127], v[84:87]
	v_add_f32_e32 v220, v220, v75
	v_add_f32_e32 v221, v221, v79
	v_mfma_f32_16x16x32_bf16 v[80:83], v[230:233], v[108:111], v[80:83]
	v_cvt_pk_bf16_f32 v216, v64, v65
	ds_read_b128 v[230:233], v246 offset:45056
	v_mfma_f32_16x16x32_bf16 v[28:31], v[234:237], v[204:207], v[28:31]
	v_cvt_pk_bf16_f32 v217, v66, v67
	v_cvt_pk_bf16_f32 v238, v68, v69
	v_mfma_f32_16x16x32_bf16 v[24:27], v[234:237], v[242:245], v[24:27]
	v_cvt_pk_bf16_f32 v239, v70, v71
	ds_read_b128 v[234:237], v210 offset:30720
	s_waitcnt lgkmcnt(6)
	v_mfma_f32_16x16x32_bf16 v[88:91], v[160:163], v[96:99], 0
	v_exp_f32_e32 v80, v80
	v_mfma_f32_16x16x32_bf16 v[92:95], v[160:163], v[112:115], 0
	v_exp_f32_e32 v84, v84
	v_mfma_f32_16x16x32_bf16 v[32:35], v[164:167], v[242:245], v[32:35]
	v_exp_f32_e32 v81, v81
	v_mfma_f32_16x16x32_bf16 v[36:39], v[164:167], v[204:207], v[36:39]
	v_exp_f32_e32 v85, v85
	s_waitcnt lgkmcnt(4)
	v_mfma_f32_16x16x32_bf16 v[92:95], v[168:171], v[116:119], v[92:95]
	v_exp_f32_e32 v82, v82
	v_mfma_f32_16x16x32_bf16 v[88:91], v[168:171], v[100:103], v[88:91]
	v_exp_f32_e32 v86, v86
	v_mfma_f32_16x16x32_bf16 v[44:47], v[172:175], v[204:207], v[44:47]
	v_exp_f32_e32 v83, v83
	v_mfma_f32_16x16x32_bf16 v[40:43], v[172:175], v[242:245], v[40:43]
	v_exp_f32_e32 v87, v87
	s_waitcnt lgkmcnt(3)
	v_mfma_f32_16x16x32_bf16 v[88:91], v[176:179], v[104:107], v[88:91]
	v_add_f32_e32 v220, v220, v80
	v_add_f32_e32 v221, v221, v84
	v_mfma_f32_16x16x32_bf16 v[92:95], v[176:179], v[120:123], v[92:95]
	v_add_f32_e32 v220, v220, v81
	s_waitcnt lgkmcnt(0)
	s_barrier
	ds_read_b128 v[160:163], v201 offset:49152
	ds_read_b128 v[164:167], v209 offset:32768
	ds_read_b128 v[168:171], v202 offset:49152
	ds_read_b128 v[172:175], v209 offset:34816
	ds_read_b128 v[176:179], v203 offset:49152
	v_mfma_f32_16x16x32_bf16 v[48:51], v[180:183], v[242:245], v[48:51]
	v_add_f32_e32 v221, v221, v85
	v_add_f32_e32 v220, v220, v82
	v_mfma_f32_16x16x32_bf16 v[52:55], v[180:183], v[204:207], v[52:55]
	v_add_f32_e32 v221, v221, v86
	ds_read_b128 v[180:183], v209 offset:36864
	v_mfma_f32_16x16x32_bf16 v[92:95], v[230:233], v[124:127], v[92:95]
	v_add_f32_e32 v220, v220, v83
	v_add_f32_e32 v221, v221, v87
	v_mfma_f32_16x16x32_bf16 v[88:91], v[230:233], v[108:111], v[88:91]
	v_cvt_pk_bf16_f32 v218, v72, v73
	ds_read_b128 v[230:233], v246 offset:49152
	v_mfma_f32_16x16x32_bf16 v[60:63], v[234:237], v[204:207], v[60:63]
	v_cvt_pk_bf16_f32 v219, v74, v75
	v_cvt_pk_bf16_f32 v240, v76, v77
	v_mfma_f32_16x16x32_bf16 v[56:59], v[234:237], v[242:245], v[56:59]
	v_cvt_pk_bf16_f32 v241, v78, v79
	ds_read_b128 v[234:237], v209 offset:38912
	s_cmp_eq_u32 s100, 0
	s_cbranch_scc1 .Lattn_pa2
	s_setprio 1
.Lattn_pa2:
	s_waitcnt lgkmcnt(6)
	v_mfma_f32_16x16x32_bf16 v[64:67], v[160:163], v[96:99], 0
	v_exp_f32_e32 v88, v88
	v_mfma_f32_16x16x32_bf16 v[68:71], v[160:163], v[112:115], 0
	v_exp_f32_e32 v92, v92
	ds_read_b128 v[160:163], v201 offset:53248
	s_add_u32 s8, s16, 0x3bc00300
	s_addc_u32 s9, s17, 0
	s_add_u32 s6, s15, 0x23a70000
	s_addc_u32 s7, s14, 0
	v_mfma_f32_16x16x32_bf16 v[0:3], v[164:167], v[216:219], v[0:3]
	v_cvt_pk_bf16_f32 v242, v80, v81
	v_mfma_f32_16x16x32_bf16 v[4:7], v[164:167], v[238:241], v[4:7]
	v_exp_f32_e32 v89, v89
	ds_read_b128 v[164:167], v209 offset:40960
	s_waitcnt vmcnt(4)
	ds_write_b128 v225, v[152:155] offset:16384
	s_waitcnt lgkmcnt(7)
	v_mfma_f32_16x16x32_bf16 v[68:71], v[168:171], v[116:119], v[68:71]
	v_exp_f32_e32 v93, v93
	v_mfma_f32_16x16x32_bf16 v[64:67], v[168:171], v[100:103], v[64:67]
	v_cvt_pk_bf16_f32 v243, v82, v83
	ds_read_b128 v[168:171], v202 offset:53248
	ds_write_b128 v226, v[156:159] offset:16384
	v_mfma_f32_16x16x32_bf16 v[12:15], v[172:175], v[238:241], v[12:15]
	v_exp_f32_e32 v90, v90
	v_mfma_f32_16x16x32_bf16 v[8:11], v[172:175], v[216:219], v[8:11]
	v_exp_f32_e32 v94, v94
	ds_read_b128 v[172:175], v209 offset:43008
	ds_write_b64 v227, v[132:133] offset:0
	s_waitcnt lgkmcnt(9)
	v_mfma_f32_16x16x32_bf16 v[64:67], v[176:179], v[104:107], v[64:67]
	v_cvt_pk_bf16_f32 v204, v84, v85
	v_mfma_f32_16x16x32_bf16 v[68:71], v[176:179], v[120:123], v[68:71]
	v_exp_f32_e32 v91, v91
	ds_read_b128 v[176:179], v203 offset:53248
	ds_write_b64 v228, v[134:135] offset:0
	v_mfma_f32_16x16x32_bf16 v[16:19], v[180:183], v[216:219], v[16:19]
	v_exp_f32_e32 v95, v95
	v_mfma_f32_16x16x32_bf16 v[20:23], v[180:183], v[238:241], v[20:23]
	v_cvt_pk_bf16_f32 v205, v86, v87
	v_add_f32_e32 v220, v220, v88
	ds_read_b128 v[180:183], v209 offset:45056
	ds_write_b64 v229, v[128:129] offset:0
	s_waitcnt lgkmcnt(11)
	v_mfma_f32_16x16x32_bf16 v[68:71], v[230:233], v[124:127], v[68:71]
	v_add_f32_e32 v221, v221, v92
	v_add_f32_e32 v220, v220, v89
	v_mfma_f32_16x16x32_bf16 v[64:67], v[230:233], v[108:111], v[64:67]
	v_add_f32_e32 v221, v221, v93
	v_cvt_pk_bf16_f32 v244, v88, v89
	ds_read_b128 v[230:233], v246 offset:53248
	ds_write_b64 v184, v[130:131] offset:0
	v_mfma_f32_16x16x32_bf16 v[28:31], v[234:237], v[238:241], v[28:31]
	v_cvt_pk_bf16_f32 v245, v90, v91
	v_cvt_pk_bf16_f32 v206, v92, v93
	v_mfma_f32_16x16x32_bf16 v[24:27], v[234:237], v[216:219], v[24:27]
	v_cvt_pk_bf16_f32 v207, v94, v95
	ds_read_b128 v[234:237], v209 offset:47104
	global_load_dwordx4 v[132:135], v198, s[8:9]
	s_waitcnt lgkmcnt(12)
	v_mfma_f32_16x16x32_bf16 v[72:75], v[160:163], v[96:99], 0
	v_add_f32_e32 v220, v220, v90
	v_add_f32_e32 v221, v221, v94
	v_mfma_f32_16x16x32_bf16 v[76:79], v[160:163], v[112:115], 0
	v_add_f32_e32 v220, v220, v91
	v_add_f32_e32 v221, v221, v95
	ds_read_b128 v[160:163], v201 offset:57344
	global_load_dwordx4 v[128:131], v199, s[8:9]
	v_mfma_f32_16x16x32_bf16 v[32:35], v[164:167], v[216:219], v[32:35]
	v_add_f32_e32 v194, v194, v220
	v_add_f32_e32 v195, v195, v221
	v_mfma_f32_16x16x32_bf16 v[36:39], v[164:167], v[238:241], v[36:39]
	v_exp_f32_e32 v64, v64
	ds_read_b128 v[164:167], v210 offset:32768
	global_load_dwordx4 v[152:155], v196, s[6:7]
	s_waitcnt lgkmcnt(10)
	v_mfma_f32_16x16x32_bf16 v[76:79], v[168:171], v[116:119], v[76:79]
	v_exp_f32_e32 v68, v68
	v_mfma_f32_16x16x32_bf16 v[72:75], v[168:171], v[100:103], v[72:75]
	v_exp_f32_e32 v65, v65
	ds_read_b128 v[168:171], v202 offset:57344
	global_load_dwordx4 v[156:159], v197, s[6:7]
	v_mfma_f32_16x16x32_bf16 v[44:47], v[172:175], v[238:241], v[44:47]
	v_exp_f32_e32 v69, v69
	v_mfma_f32_16x16x32_bf16 v[40:43], v[172:175], v[216:219], v[40:43]
	v_exp_f32_e32 v66, v66
	ds_read_b128 v[172:175], v210 offset:34816
	s_waitcnt lgkmcnt(8)
	v_mfma_f32_16x16x32_bf16 v[72:75], v[176:179], v[104:107], v[72:75]
	v_exp_f32_e32 v70, v70
	v_mfma_f32_16x16x32_bf16 v[76:79], v[176:179], v[120:123], v[76:79]
	v_exp_f32_e32 v67, v67
	ds_read_b128 v[176:179], v203 offset:57344
	v_mfma_f32_16x16x32_bf16 v[48:51], v[180:183], v[216:219], v[48:51]
	v_exp_f32_e32 v71, v71
	v_mfma_f32_16x16x32_bf16 v[52:55], v[180:183], v[238:241], v[52:55]
	v_add_f32_e32 v220, v64, v65
	ds_read_b128 v[180:183], v210 offset:36864
	s_waitcnt lgkmcnt(6)
	v_mfma_f32_16x16x32_bf16 v[76:79], v[230:233], v[124:127], v[76:79]
	v_add_f32_e32 v221, v68, v69
	v_mfma_f32_16x16x32_bf16 v[72:75], v[230:233], v[108:111], v[72:75]
	v_add_f32_e32 v220, v220, v66
	ds_read_b128 v[230:233], v246 offset:57344
	v_mfma_f32_16x16x32_bf16 v[60:63], v[234:237], v[238:241], v[60:63]
	v_add_f32_e32 v221, v221, v70
	v_add_f32_e32 v220, v220, v67
	v_mfma_f32_16x16x32_bf16 v[56:59], v[234:237], v[216:219], v[56:59]
	v_add_f32_e32 v221, v221, v71
	ds_read_b128 v[234:237], v210 offset:38912
	s_waitcnt lgkmcnt(6)
	v_mfma_f32_16x16x32_bf16 v[80:83], v[160:163], v[96:99], 0
	v_exp_f32_e32 v72, v72
	v_mfma_f32_16x16x32_bf16 v[84:87], v[160:163], v[112:115], 0
	v_exp_f32_e32 v76, v76
	ds_read_b128 v[160:163], v201 offset:61440
	v_mfma_f32_16x16x32_bf16 v[0:3], v[164:167], v[242:245], v[0:3]
	v_exp_f32_e32 v73, v73
	v_mfma_f32_16x16x32_bf16 v[4:7], v[164:167], v[204:207], v[4:7]
	v_exp_f32_e32 v77, v77
	ds_read_b128 v[164:167], v210 offset:40960
	s_waitcnt lgkmcnt(6)
	v_mfma_f32_16x16x32_bf16 v[84:87], v[168:171], v[116:119], v[84:87]
	v_exp_f32_e32 v74, v74
	v_mfma_f32_16x16x32_bf16 v[80:83], v[168:171], v[100:103], v[80:83]
	v_exp_f32_e32 v78, v78
	ds_read_b128 v[168:171], v202 offset:61440
	v_mfma_f32_16x16x32_bf16 v[12:15], v[172:175], v[204:207], v[12:15]
	v_exp_f32_e32 v75, v75
	v_mfma_f32_16x16x32_bf16 v[8:11], v[172:175], v[242:245], v[8:11]
	v_exp_f32_e32 v79, v79
	ds_read_b128 v[172:175], v210 offset:43008
	s_waitcnt lgkmcnt(6)
	v_mfma_f32_16x16x32_bf16 v[80:83], v[176:179], v[104:107], v[80:83]
	v_add_f32_e32 v220, v220, v72
	v_add_f32_e32 v221, v221, v76
	v_mfma_f32_16x16x32_bf16 v[84:87], v[176:179], v[120:123], v[84:87]
	v_add_f32_e32 v220, v220, v73
	ds_read_b128 v[176:179], v203 offset:61440
	v_mfma_f32_16x16x32_bf16 v[16:19], v[180:183], v[242:245], v[16:19]
	v_add_f32_e32 v221, v221, v77
	v_add_f32_e32 v220, v220, v74
	v_mfma_f32_16x16x32_bf16 v[20:23], v[180:183], v[204:207], v[20:23]
	v_add_f32_e32 v221, v221, v78
	ds_read_b128 v[180:183], v210 offset:45056
	s_waitcnt lgkmcnt(6)
	v_mfma_f32_16x16x32_bf16 v[84:87], v[230:233], v[124:127], v[84:87]
	v_add_f32_e32 v220, v220, v75
	v_add_f32_e32 v221, v221, v79
	v_mfma_f32_16x16x32_bf16 v[80:83], v[230:233], v[108:111], v[80:83]
	v_cvt_pk_bf16_f32 v216, v64, v65
	ds_read_b128 v[230:233], v246 offset:61440
	v_mfma_f32_16x16x32_bf16 v[28:31], v[234:237], v[204:207], v[28:31]
	v_cvt_pk_bf16_f32 v217, v66, v67
	v_cvt_pk_bf16_f32 v238, v68, v69
	v_mfma_f32_16x16x32_bf16 v[24:27], v[234:237], v[242:245], v[24:27]
	v_cvt_pk_bf16_f32 v239, v70, v71
	ds_read_b128 v[234:237], v210 offset:47104
	s_waitcnt lgkmcnt(6)
	v_mfma_f32_16x16x32_bf16 v[88:91], v[160:163], v[96:99], 0
	v_exp_f32_e32 v80, v80
	v_mfma_f32_16x16x32_bf16 v[92:95], v[160:163], v[112:115], 0
	v_exp_f32_e32 v84, v84
	ds_read_b128 v[160:163], v201 offset:0
	v_mfma_f32_16x16x32_bf16 v[32:35], v[164:167], v[242:245], v[32:35]
	v_exp_f32_e32 v81, v81
	v_mfma_f32_16x16x32_bf16 v[36:39], v[164:167], v[204:207], v[36:39]
	v_exp_f32_e32 v85, v85
	ds_read_b128 v[164:167], v209 offset:49152
	s_waitcnt lgkmcnt(6)
	v_mfma_f32_16x16x32_bf16 v[92:95], v[168:171], v[116:119], v[92:95]
	v_exp_f32_e32 v82, v82
	v_mfma_f32_16x16x32_bf16 v[88:91], v[168:171], v[100:103], v[88:91]
	v_exp_f32_e32 v86, v86
	ds_read_b128 v[168:171], v202 offset:0
	v_mfma_f32_16x16x32_bf16 v[44:47], v[172:175], v[204:207], v[44:47]
	v_exp_f32_e32 v83, v83
	v_mfma_f32_16x16x32_bf16 v[40:43], v[172:175], v[242:245], v[40:43]
	v_exp_f32_e32 v87, v87
	ds_read_b128 v[172:175], v209 offset:51200
	s_waitcnt lgkmcnt(6)
	v_mfma_f32_16x16x32_bf16 v[88:91], v[176:179], v[104:107], v[88:91]
	v_add_f32_e32 v220, v220, v80
	v_add_f32_e32 v221, v221, v84
	v_mfma_f32_16x16x32_bf16 v[92:95], v[176:179], v[120:123], v[92:95]
	v_add_f32_e32 v220, v220, v81
	ds_read_b128 v[176:179], v203 offset:0
	v_mfma_f32_16x16x32_bf16 v[48:51], v[180:183], v[242:245], v[48:51]
	v_add_f32_e32 v221, v221, v85
	v_add_f32_e32 v220, v220, v82
	v_mfma_f32_16x16x32_bf16 v[52:55], v[180:183], v[204:207], v[52:55]
	v_add_f32_e32 v221, v221, v86
	ds_read_b128 v[180:183], v209 offset:53248
	s_waitcnt lgkmcnt(6)
	v_mfma_f32_16x16x32_bf16 v[92:95], v[230:233], v[124:127], v[92:95]
	v_add_f32_e32 v220, v220, v83
	v_add_f32_e32 v221, v221, v87
	v_mfma_f32_16x16x32_bf16 v[88:91], v[230:233], v[108:111], v[88:91]
	v_cvt_pk_bf16_f32 v218, v72, v73
	ds_read_b128 v[230:233], v246 offset:0
	v_mfma_f32_16x16x32_bf16 v[60:63], v[234:237], v[204:207], v[60:63]
	v_cvt_pk_bf16_f32 v219, v74, v75
	v_cvt_pk_bf16_f32 v240, v76, v77
	v_mfma_f32_16x16x32_bf16 v[56:59], v[234:237], v[242:245], v[56:59]
	v_cvt_pk_bf16_f32 v241, v78, v79
	ds_read_b128 v[234:237], v209 offset:55296
	s_setprio 0
	s_waitcnt lgkmcnt(6)
	v_mfma_f32_16x16x32_bf16 v[64:67], v[160:163], v[96:99], 0
	v_exp_f32_e32 v88, v88
	v_mfma_f32_16x16x32_bf16 v[68:71], v[160:163], v[112:115], 0
	v_exp_f32_e32 v92, v92
	ds_read_b128 v[160:163], v201 offset:4096
	s_add_u32 s8, s16, 0x3bc00380
	s_addc_u32 s9, s17, 0
	s_add_u32 s6, s15, 0x23a80000
	s_addc_u32 s7, s14, 0
	v_mfma_f32_16x16x32_bf16 v[0:3], v[164:167], v[216:219], v[0:3]
	v_cvt_pk_bf16_f32 v242, v80, v81
	v_mfma_f32_16x16x32_bf16 v[4:7], v[164:167], v[238:241], v[4:7]
	v_exp_f32_e32 v89, v89
	ds_read_b128 v[164:167], v209 offset:57344
	s_waitcnt vmcnt(4)
	ds_write_b128 v225, v[136:139] offset:32768
	s_waitcnt lgkmcnt(7)
	v_mfma_f32_16x16x32_bf16 v[68:71], v[168:171], v[116:119], v[68:71]
	v_exp_f32_e32 v93, v93
	v_mfma_f32_16x16x32_bf16 v[64:67], v[168:171], v[100:103], v[64:67]
	v_cvt_pk_bf16_f32 v243, v82, v83
	ds_read_b128 v[168:171], v202 offset:4096
	ds_write_b128 v226, v[140:143] offset:32768
	v_mfma_f32_16x16x32_bf16 v[12:15], v[172:175], v[238:241], v[12:15]
	v_exp_f32_e32 v90, v90
	v_mfma_f32_16x16x32_bf16 v[8:11], v[172:175], v[216:219], v[8:11]
	v_exp_f32_e32 v94, v94
	ds_read_b128 v[172:175], v209 offset:59392
	ds_write_b64 v227, v[148:149] offset:16384
	s_waitcnt lgkmcnt(9)
	v_mfma_f32_16x16x32_bf16 v[64:67], v[176:179], v[104:107], v[64:67]
	v_cvt_pk_bf16_f32 v204, v84, v85
	v_mfma_f32_16x16x32_bf16 v[68:71], v[176:179], v[120:123], v[68:71]
	v_exp_f32_e32 v91, v91
	ds_read_b128 v[176:179], v203 offset:4096
	ds_write_b64 v228, v[150:151] offset:16384
	v_mfma_f32_16x16x32_bf16 v[16:19], v[180:183], v[216:219], v[16:19]
	v_exp_f32_e32 v95, v95
	v_mfma_f32_16x16x32_bf16 v[20:23], v[180:183], v[238:241], v[20:23]
	v_cvt_pk_bf16_f32 v205, v86, v87
	v_add_f32_e32 v220, v220, v88
	ds_read_b128 v[180:183], v209 offset:61440
	ds_write_b64 v229, v[144:145] offset:16384
	s_waitcnt lgkmcnt(11)
	v_mfma_f32_16x16x32_bf16 v[68:71], v[230:233], v[124:127], v[68:71]
	v_add_f32_e32 v221, v221, v92
	v_add_f32_e32 v220, v220, v89
	v_mfma_f32_16x16x32_bf16 v[64:67], v[230:233], v[108:111], v[64:67]
	v_add_f32_e32 v221, v221, v93
	v_cvt_pk_bf16_f32 v244, v88, v89
	ds_read_b128 v[230:233], v246 offset:4096
	ds_write_b64 v184, v[146:147] offset:16384
	v_mfma_f32_16x16x32_bf16 v[28:31], v[234:237], v[238:241], v[28:31]
	v_cvt_pk_bf16_f32 v245, v90, v91
	v_cvt_pk_bf16_f32 v206, v92, v93
	v_mfma_f32_16x16x32_bf16 v[24:27], v[234:237], v[216:219], v[24:27]
	v_cvt_pk_bf16_f32 v207, v94, v95
	ds_read_b128 v[234:237], v209 offset:63488
	global_load_dwordx4 v[148:151], v198, s[8:9]
	s_waitcnt lgkmcnt(12)
	v_mfma_f32_16x16x32_bf16 v[72:75], v[160:163], v[96:99], 0
	v_add_f32_e32 v220, v220, v90
	v_add_f32_e32 v221, v221, v94
	v_mfma_f32_16x16x32_bf16 v[76:79], v[160:163], v[112:115], 0
	v_add_f32_e32 v220, v220, v91
	v_add_f32_e32 v221, v221, v95
	ds_read_b128 v[160:163], v201 offset:8192
	global_load_dwordx4 v[144:147], v199, s[8:9]
	v_mfma_f32_16x16x32_bf16 v[32:35], v[164:167], v[216:219], v[32:35]
	v_add_f32_e32 v194, v194, v220
	v_add_f32_e32 v195, v195, v221
	v_mfma_f32_16x16x32_bf16 v[36:39], v[164:167], v[238:241], v[36:39]
	v_exp_f32_e32 v64, v64
	ds_read_b128 v[164:167], v210 offset:49152
	global_load_dwordx4 v[136:139], v196, s[6:7]
	s_waitcnt lgkmcnt(10)
	v_mfma_f32_16x16x32_bf16 v[76:79], v[168:171], v[116:119], v[76:79]
	v_exp_f32_e32 v68, v68
	v_mfma_f32_16x16x32_bf16 v[72:75], v[168:171], v[100:103], v[72:75]
	v_exp_f32_e32 v65, v65
	ds_read_b128 v[168:171], v202 offset:8192
	global_load_dwordx4 v[140:143], v197, s[6:7]
	v_mfma_f32_16x16x32_bf16 v[44:47], v[172:175], v[238:241], v[44:47]
	v_exp_f32_e32 v69, v69
	v_mfma_f32_16x16x32_bf16 v[40:43], v[172:175], v[216:219], v[40:43]
	v_exp_f32_e32 v66, v66
	ds_read_b128 v[172:175], v210 offset:51200
	s_waitcnt lgkmcnt(8)
	v_mfma_f32_16x16x32_bf16 v[72:75], v[176:179], v[104:107], v[72:75]
	v_exp_f32_e32 v70, v70
	v_mfma_f32_16x16x32_bf16 v[76:79], v[176:179], v[120:123], v[76:79]
	v_exp_f32_e32 v67, v67
	ds_read_b128 v[176:179], v203 offset:8192
	v_mfma_f32_16x16x32_bf16 v[48:51], v[180:183], v[216:219], v[48:51]
	v_exp_f32_e32 v71, v71
	v_mfma_f32_16x16x32_bf16 v[52:55], v[180:183], v[238:241], v[52:55]
	v_add_f32_e32 v220, v64, v65
	ds_read_b128 v[180:183], v210 offset:53248
	s_waitcnt lgkmcnt(6)
	v_mfma_f32_16x16x32_bf16 v[76:79], v[230:233], v[124:127], v[76:79]
	v_add_f32_e32 v221, v68, v69
	v_mfma_f32_16x16x32_bf16 v[72:75], v[230:233], v[108:111], v[72:75]
	v_add_f32_e32 v220, v220, v66
	ds_read_b128 v[230:233], v246 offset:8192
	v_mfma_f32_16x16x32_bf16 v[60:63], v[234:237], v[238:241], v[60:63]
	v_add_f32_e32 v221, v221, v70
	v_add_f32_e32 v220, v220, v67
	v_mfma_f32_16x16x32_bf16 v[56:59], v[234:237], v[216:219], v[56:59]
	v_add_f32_e32 v221, v221, v71
	ds_read_b128 v[234:237], v210 offset:55296
	s_waitcnt lgkmcnt(6)
	v_mfma_f32_16x16x32_bf16 v[80:83], v[160:163], v[96:99], 0
	v_exp_f32_e32 v72, v72
	v_mfma_f32_16x16x32_bf16 v[84:87], v[160:163], v[112:115], 0
	v_exp_f32_e32 v76, v76
	ds_read_b128 v[160:163], v201 offset:12288
	v_mfma_f32_16x16x32_bf16 v[0:3], v[164:167], v[242:245], v[0:3]
	v_exp_f32_e32 v73, v73
	v_mfma_f32_16x16x32_bf16 v[4:7], v[164:167], v[204:207], v[4:7]
	v_exp_f32_e32 v77, v77
	ds_read_b128 v[164:167], v210 offset:57344
	s_waitcnt lgkmcnt(6)
	v_mfma_f32_16x16x32_bf16 v[84:87], v[168:171], v[116:119], v[84:87]
	v_exp_f32_e32 v74, v74
	v_mfma_f32_16x16x32_bf16 v[80:83], v[168:171], v[100:103], v[80:83]
	v_exp_f32_e32 v78, v78
	ds_read_b128 v[168:171], v202 offset:12288
	v_mfma_f32_16x16x32_bf16 v[12:15], v[172:175], v[204:207], v[12:15]
	v_exp_f32_e32 v75, v75
	v_mfma_f32_16x16x32_bf16 v[8:11], v[172:175], v[242:245], v[8:11]
	v_exp_f32_e32 v79, v79
	ds_read_b128 v[172:175], v210 offset:59392
	s_waitcnt lgkmcnt(6)
	v_mfma_f32_16x16x32_bf16 v[80:83], v[176:179], v[104:107], v[80:83]
	v_add_f32_e32 v220, v220, v72
	v_add_f32_e32 v221, v221, v76
	v_mfma_f32_16x16x32_bf16 v[84:87], v[176:179], v[120:123], v[84:87]
	v_add_f32_e32 v220, v220, v73
	ds_read_b128 v[176:179], v203 offset:12288
	s_add_u32 s10, s10, 0x200
	s_addc_u32 s11, s11, 0
	s_add_u32 s12, s12, 0x40000
	s_addc_u32 s13, s13, 0
	s_add_i32 s4, s4, 4
	s_cmpk_lt_u32 s4, 0x104
	s_cselect_b64 s[6:7], -1, 0
	s_and_b64 s[6:7], s[0:1], s[6:7]
	s_and_b64 vcc, exec, s[6:7]
	v_mfma_f32_16x16x32_bf16 v[16:19], v[180:183], v[242:245], v[16:19]
	v_add_f32_e32 v221, v221, v77
	v_add_f32_e32 v220, v220, v74
	v_mfma_f32_16x16x32_bf16 v[20:23], v[180:183], v[204:207], v[20:23]
	v_add_f32_e32 v221, v221, v78
	ds_read_b128 v[180:183], v210 offset:61440
	s_waitcnt lgkmcnt(6)
	v_mfma_f32_16x16x32_bf16 v[84:87], v[230:233], v[124:127], v[84:87]
	v_add_f32_e32 v220, v220, v75
	v_add_f32_e32 v221, v221, v79
	v_mfma_f32_16x16x32_bf16 v[80:83], v[230:233], v[108:111], v[80:83]
	v_cvt_pk_bf16_f32 v216, v64, v65
	ds_read_b128 v[230:233], v246 offset:12288
	v_mfma_f32_16x16x32_bf16 v[28:31], v[234:237], v[204:207], v[28:31]
	v_cvt_pk_bf16_f32 v217, v66, v67
	v_cvt_pk_bf16_f32 v238, v68, v69
	v_mfma_f32_16x16x32_bf16 v[24:27], v[234:237], v[242:245], v[24:27]
	v_cvt_pk_bf16_f32 v239, v70, v71
	ds_read_b128 v[234:237], v210 offset:63488
	s_waitcnt lgkmcnt(6)
	v_mfma_f32_16x16x32_bf16 v[88:91], v[160:163], v[96:99], 0
	v_exp_f32_e32 v80, v80
	v_mfma_f32_16x16x32_bf16 v[92:95], v[160:163], v[112:115], 0
	v_exp_f32_e32 v84, v84
	v_mfma_f32_16x16x32_bf16 v[32:35], v[164:167], v[242:245], v[32:35]
	v_exp_f32_e32 v81, v81
	v_mfma_f32_16x16x32_bf16 v[36:39], v[164:167], v[204:207], v[36:39]
	v_exp_f32_e32 v85, v85
	s_waitcnt lgkmcnt(4)
	v_mfma_f32_16x16x32_bf16 v[92:95], v[168:171], v[116:119], v[92:95]
	v_exp_f32_e32 v82, v82
	v_mfma_f32_16x16x32_bf16 v[88:91], v[168:171], v[100:103], v[88:91]
	v_exp_f32_e32 v86, v86
	v_mfma_f32_16x16x32_bf16 v[44:47], v[172:175], v[204:207], v[44:47]
	v_exp_f32_e32 v83, v83
	v_mfma_f32_16x16x32_bf16 v[40:43], v[172:175], v[242:245], v[40:43]
	v_exp_f32_e32 v87, v87
	s_waitcnt lgkmcnt(3)
	v_mfma_f32_16x16x32_bf16 v[88:91], v[176:179], v[104:107], v[88:91]
	v_add_f32_e32 v220, v220, v80
	v_add_f32_e32 v221, v221, v84
	v_mfma_f32_16x16x32_bf16 v[92:95], v[176:179], v[120:123], v[92:95]
	v_add_f32_e32 v220, v220, v81
	s_waitcnt lgkmcnt(0)
	s_barrier
	ds_read_b128 v[160:163], v201 offset:16384
	ds_read_b128 v[164:167], v209 offset:0
	ds_read_b128 v[168:171], v202 offset:16384
	ds_read_b128 v[172:175], v209 offset:2048
	ds_read_b128 v[176:179], v203 offset:16384
	v_mfma_f32_16x16x32_bf16 v[48:51], v[180:183], v[242:245], v[48:51]
	v_add_f32_e32 v221, v221, v85
	v_add_f32_e32 v220, v220, v82
	v_mfma_f32_16x16x32_bf16 v[52:55], v[180:183], v[204:207], v[52:55]
	v_add_f32_e32 v221, v221, v86
	ds_read_b128 v[180:183], v209 offset:4096
	v_mfma_f32_16x16x32_bf16 v[92:95], v[230:233], v[124:127], v[92:95]
	v_add_f32_e32 v220, v220, v83
	v_add_f32_e32 v221, v221, v87
	v_mfma_f32_16x16x32_bf16 v[88:91], v[230:233], v[108:111], v[88:91]
	v_cvt_pk_bf16_f32 v218, v72, v73
	ds_read_b128 v[230:233], v246 offset:16384
	v_mfma_f32_16x16x32_bf16 v[60:63], v[234:237], v[204:207], v[60:63]
	v_cvt_pk_bf16_f32 v219, v74, v75
	v_cvt_pk_bf16_f32 v240, v76, v77
	v_mfma_f32_16x16x32_bf16 v[56:59], v[234:237], v[242:245], v[56:59]
	v_cvt_pk_bf16_f32 v241, v78, v79
	ds_read_b128 v[234:237], v209 offset:6144
	s_cbranch_vccnz .LBB0_734
	s_setprio 0
	s_waitcnt vmcnt(0)
	s_nop 7
	s_nop 7
	ds_swizzle_b32 v64, v194 offset:swizzle(SWAP,16)
	s_waitcnt lgkmcnt(0)
	v_add_f32_e32 v194, v194, v64
	v_mov_b32_e32 v65, v194
	s_nop 1
	v_permlane32_swap_b32_e32 v194, v65
	v_add_f32_e32 v194, v194, v65
	s_nop 0
	v_rcp_f32_e32 v66, v194
	ds_swizzle_b32 v64, v195 offset:swizzle(SWAP,16)
	s_waitcnt lgkmcnt(0)
	v_add_f32_e32 v195, v195, v64
	v_mov_b32_e32 v65, v195
	s_nop 1
	v_permlane32_swap_b32_e32 v195, v65
	v_add_f32_e32 v195, v195, v65
	s_nop 0
	v_rcp_f32_e32 v67, v195
	v_readlane_b32 s100, v250, 8
	v_mbcnt_lo_u32_b32 v68, -1, 0
	v_mbcnt_hi_u32_b32 v68, -1, v68
	v_and_b32_e32 v69, 15, v68
	v_lshrrev_b32_e32 v70, 4, v68
	s_lshr_b32 s101, s100, 1
	v_add_u32_e32 v69, s101, v69
	v_lshlrev_b32_e32 v69, 12, v69
	v_and_b32_e32 v71, 1, v70
	v_lshlrev_b32_e32 v71, 5, v71
	v_and_b32_e32 v70, 2, v70
	v_lshl_add_u32 v71, v70, 3, v71
	v_add_u32_e32 v70, v69, v71
	v_add_u32_e32 v71, 0x10000, v70
	v_mul_f32_e32 v0, v0, v66
	v_mul_f32_e32 v1, v1, v66
	v_mul_f32_e32 v2, v2, v66
	v_mul_f32_e32 v3, v3, v66
	v_mul_f32_e32 v8, v8, v66
	v_mul_f32_e32 v9, v9, v66
	v_mul_f32_e32 v10, v10, v66
	v_mul_f32_e32 v11, v11, v66
	v_cvt_pk_bf16_f32 v72, v0, v1
	v_cvt_pk_bf16_f32 v73, v2, v3
	v_cvt_pk_bf16_f32 v74, v8, v9
	v_cvt_pk_bf16_f32 v75, v10, v11
	s_nop 1
	v_permlane16_swap_b32_e32 v72, v74
	v_permlane16_swap_b32_e32 v73, v75
	s_nop 1
	global_store_dwordx4 v70, v[72:75], s[58:59] offset:0
	v_mul_f32_e32 v16, v16, v66
	v_mul_f32_e32 v17, v17, v66
	v_mul_f32_e32 v18, v18, v66
	v_mul_f32_e32 v19, v19, v66
	v_mul_f32_e32 v24, v24, v66
	v_mul_f32_e32 v25, v25, v66
	v_mul_f32_e32 v26, v26, v66
	v_mul_f32_e32 v27, v27, v66
	v_cvt_pk_bf16_f32 v76, v16, v17
	v_cvt_pk_bf16_f32 v77, v18, v19
	v_cvt_pk_bf16_f32 v78, v24, v25
	v_cvt_pk_bf16_f32 v79, v26, v27
	s_nop 1
	v_permlane16_swap_b32_e32 v76, v78
	v_permlane16_swap_b32_e32 v77, v79
	s_nop 1
	global_store_dwordx4 v70, v[76:79], s[58:59] offset:64
	v_mul_f32_e32 v32, v32, v66
	v_mul_f32_e32 v33, v33, v66
	v_mul_f32_e32 v34, v34, v66
	v_mul_f32_e32 v35, v35, v66
	v_mul_f32_e32 v40, v40, v66
	v_mul_f32_e32 v41, v41, v66
	v_mul_f32_e32 v42, v42, v66
	v_mul_f32_e32 v43, v43, v66
	v_cvt_pk_bf16_f32 v80, v32, v33
	v_cvt_pk_bf16_f32 v81, v34, v35
	v_cvt_pk_bf16_f32 v82, v40, v41
	v_cvt_pk_bf16_f32 v83, v42, v43
	s_nop 1
	v_permlane16_swap_b32_e32 v80, v82
	v_permlane16_swap_b32_e32 v81, v83
	s_nop 1
	global_store_dwordx4 v70, v[80:83], s[58:59] offset:128
	v_mul_f32_e32 v48, v48, v66
	v_mul_f32_e32 v49, v49, v66
	v_mul_f32_e32 v50, v50, v66
	v_mul_f32_e32 v51, v51, v66
	v_mul_f32_e32 v56, v56, v66
	v_mul_f32_e32 v57, v57, v66
	v_mul_f32_e32 v58, v58, v66
	v_mul_f32_e32 v59, v59, v66
	v_cvt_pk_bf16_f32 v84, v48, v49
	v_cvt_pk_bf16_f32 v85, v50, v51
	v_cvt_pk_bf16_f32 v86, v56, v57
	v_cvt_pk_bf16_f32 v87, v58, v59
	s_nop 1
	v_permlane16_swap_b32_e32 v84, v86
	v_permlane16_swap_b32_e32 v85, v87
	s_nop 1
	global_store_dwordx4 v70, v[84:87], s[58:59] offset:192
	v_mul_f32_e32 v4, v4, v67
	v_mul_f32_e32 v5, v5, v67
	v_mul_f32_e32 v6, v6, v67
	v_mul_f32_e32 v7, v7, v67
	v_mul_f32_e32 v12, v12, v67
	v_mul_f32_e32 v13, v13, v67
	v_mul_f32_e32 v14, v14, v67
	v_mul_f32_e32 v15, v15, v67
	v_cvt_pk_bf16_f32 v88, v4, v5
	v_cvt_pk_bf16_f32 v89, v6, v7
	v_cvt_pk_bf16_f32 v90, v12, v13
	v_cvt_pk_bf16_f32 v91, v14, v15
	s_nop 1
	v_permlane16_swap_b32_e32 v88, v90
	v_permlane16_swap_b32_e32 v89, v91
	s_nop 1
	global_store_dwordx4 v71, v[88:91], s[58:59] offset:0
	v_mul_f32_e32 v20, v20, v67
	v_mul_f32_e32 v21, v21, v67
	v_mul_f32_e32 v22, v22, v67
	v_mul_f32_e32 v23, v23, v67
	v_mul_f32_e32 v28, v28, v67
	v_mul_f32_e32 v29, v29, v67
	v_mul_f32_e32 v30, v30, v67
	v_mul_f32_e32 v31, v31, v67
	v_cvt_pk_bf16_f32 v92, v20, v21
	v_cvt_pk_bf16_f32 v93, v22, v23
	v_cvt_pk_bf16_f32 v94, v28, v29
	v_cvt_pk_bf16_f32 v95, v30, v31
	s_nop 1
	v_permlane16_swap_b32_e32 v92, v94
	v_permlane16_swap_b32_e32 v93, v95
	s_nop 1
	global_store_dwordx4 v71, v[92:95], s[58:59] offset:64
	v_mul_f32_e32 v36, v36, v67
	v_mul_f32_e32 v37, v37, v67
	v_mul_f32_e32 v38, v38, v67
	v_mul_f32_e32 v39, v39, v67
	v_mul_f32_e32 v44, v44, v67
	v_mul_f32_e32 v45, v45, v67
	v_mul_f32_e32 v46, v46, v67
	v_mul_f32_e32 v47, v47, v67
	v_cvt_pk_bf16_f32 v72, v36, v37
	v_cvt_pk_bf16_f32 v73, v38, v39
	v_cvt_pk_bf16_f32 v74, v44, v45
	v_cvt_pk_bf16_f32 v75, v46, v47
	s_nop 1
	v_permlane16_swap_b32_e32 v72, v74
	v_permlane16_swap_b32_e32 v73, v75
	s_nop 1
	global_store_dwordx4 v71, v[72:75], s[58:59] offset:128
	v_mul_f32_e32 v52, v52, v67
	v_mul_f32_e32 v53, v53, v67
	v_mul_f32_e32 v54, v54, v67
	v_mul_f32_e32 v55, v55, v67
	v_mul_f32_e32 v60, v60, v67
	v_mul_f32_e32 v61, v61, v67
	v_mul_f32_e32 v62, v62, v67
	v_mul_f32_e32 v63, v63, v67
	v_cvt_pk_bf16_f32 v76, v52, v53
	v_cvt_pk_bf16_f32 v77, v54, v55
	v_cvt_pk_bf16_f32 v78, v60, v61
	v_cvt_pk_bf16_f32 v79, v62, v63
	s_nop 1
	v_permlane16_swap_b32_e32 v76, v78
	v_permlane16_swap_b32_e32 v77, v79
	s_nop 1
	global_store_dwordx4 v71, v[76:79], s[58:59] offset:192
	s_barrier
